# speedup vs baseline: 1.0072x; 1.0072x over previous
_Z6gat_k2PKDF16_S0_S0_PKfPf:
	s_load_dwordx8 s[4:11], s[0:1], 0x0
	s_load_dwordx2 s[12:13], s[0:1], 0x20
	v_readfirstlane_b32 s14, v0
	v_and_b32_e32 v46, 63, v0
	v_lshlrev_b32_e32 v1, 4, v46
	s_and_b32 s16, s2, 1
	s_bfe_u32 s17, s2, 0x60003
	s_lshr_b32 s18, s2, 1
	s_lshr_b32 s15, s14, 6
	s_lshl_b32 s19, s16, 19
	s_lshl_b32 s23, s15, 16
	s_add_u32 s19, s19, s23
	s_lshl_b32 s23, s15, 11
	v_add_u32_e32 v47, s23, v1
	v_and_b32_e32 v44, 31, v0
	v_lshlrev_b32_e32 v45, 2, v44
	s_lshl_b32 s23, s18, 8
	v_add_u32_e32 v45, s23, v45
	s_waitcnt lgkmcnt(0)
	global_load_dword v42, v45, s[10:11]
	global_load_dword v43, v45, s[10:11] offset:128
	global_load_dwordx4 v[48:51], v47, s[6:7]
	global_load_dwordx4 v[52:55], v47, s[6:7] offset:1024
	global_load_dwordx4 v[56:59], v47, s[8:9]
	global_load_dwordx4 v[60:63], v47, s[8:9] offset:1024
	s_add_u32 s20, s4, s19
	s_addc_u32 s21, s5, 0
	s_add_u32 s23, s17, 0
	s_and_b32 s23, s23, 63
	s_lshl_b32 s23, s23, 10
	s_add_u32 s24, s20, s23
	s_addc_u32 s25, s21, 0
	global_load_dwordx4 v[64:67], v1, s[24:25]
	s_add_u32 s23, s17, 1
	s_and_b32 s23, s23, 63
	s_lshl_b32 s23, s23, 10
	s_add_u32 s24, s20, s23
	s_addc_u32 s25, s21, 0
	global_load_dwordx4 v[68:71], v1, s[24:25]
	s_add_u32 s23, s17, 2
	s_and_b32 s23, s23, 63
	s_lshl_b32 s23, s23, 10
	s_add_u32 s24, s20, s23
	s_addc_u32 s25, s21, 0
	global_load_dwordx4 v[72:75], v1, s[24:25]
	s_add_u32 s23, s17, 3
	s_and_b32 s23, s23, 63
	s_lshl_b32 s23, s23, 10
	s_add_u32 s24, s20, s23
	s_addc_u32 s25, s21, 0
	global_load_dwordx4 v[76:79], v1, s[24:25]
	s_add_u32 s23, s17, 4
	s_and_b32 s23, s23, 63
	s_lshl_b32 s23, s23, 10
	s_add_u32 s24, s20, s23
	s_addc_u32 s25, s21, 0
	global_load_dwordx4 v[80:83], v1, s[24:25]
	s_add_u32 s23, s17, 5
	s_and_b32 s23, s23, 63
	s_lshl_b32 s23, s23, 10
	s_add_u32 s24, s20, s23
	s_addc_u32 s25, s21, 0
	global_load_dwordx4 v[84:87], v1, s[24:25]
	s_add_u32 s23, s17, 6
	s_and_b32 s23, s23, 63
	s_lshl_b32 s23, s23, 10
	s_add_u32 s24, s20, s23
	s_addc_u32 s25, s21, 0
	global_load_dwordx4 v[88:91], v1, s[24:25]
	s_add_u32 s23, s17, 7
	s_and_b32 s23, s23, 63
	s_lshl_b32 s23, s23, 10
	s_add_u32 s24, s20, s23
	s_addc_u32 s25, s21, 0
	global_load_dwordx4 v[92:95], v1, s[24:25]
	v_accvgpr_write_b32 a0, 0
	v_accvgpr_write_b32 a1, 0
	v_accvgpr_write_b32 a2, 0
	v_accvgpr_write_b32 a3, 0
	v_accvgpr_write_b32 a4, 0
	v_accvgpr_write_b32 a5, 0
	v_accvgpr_write_b32 a6, 0
	v_accvgpr_write_b32 a7, 0
	v_accvgpr_write_b32 a8, 0
	v_accvgpr_write_b32 a9, 0
	v_accvgpr_write_b32 a10, 0
	v_accvgpr_write_b32 a11, 0
	v_accvgpr_write_b32 a12, 0
	v_accvgpr_write_b32 a13, 0
	v_accvgpr_write_b32 a14, 0
	v_accvgpr_write_b32 a15, 0
	v_accvgpr_write_b32 a16, 0
	v_accvgpr_write_b32 a17, 0
	v_accvgpr_write_b32 a18, 0
	v_accvgpr_write_b32 a19, 0
	v_accvgpr_write_b32 a20, 0
	v_accvgpr_write_b32 a21, 0
	v_accvgpr_write_b32 a22, 0
	v_accvgpr_write_b32 a23, 0
	v_accvgpr_write_b32 a24, 0
	v_accvgpr_write_b32 a25, 0
	v_accvgpr_write_b32 a26, 0
	v_accvgpr_write_b32 a27, 0
	v_accvgpr_write_b32 a28, 0
	v_accvgpr_write_b32 a29, 0
	v_accvgpr_write_b32 a30, 0
	v_accvgpr_write_b32 a31, 0
	v_accvgpr_write_b32 a32, 0
	v_accvgpr_write_b32 a33, 0
	v_accvgpr_write_b32 a34, 0
	v_accvgpr_write_b32 a35, 0
	v_accvgpr_write_b32 a36, 0
	v_accvgpr_write_b32 a37, 0
	v_accvgpr_write_b32 a38, 0
	v_accvgpr_write_b32 a39, 0
	v_mov_b32_e32 v2, 0
	v_mov_b32_e32 v3, 0
	v_mov_b32_e32 v4, 0
	v_mov_b32_e32 v5, 0
	v_lshrrev_b32_e32 v44, 1, v46
	v_subrev_u32_e32 v44, s17, v44
	v_and_b32_e32 v44, 63, v44
	v_lshlrev_b32_e32 v44, 5, v44
	v_and_b32_e32 v45, 1, v46
	v_lshl_or_b32 v44, v45, 4, v44
	v_xor_b32_e32 v45, 0x400, v44
	s_mul_i32 s23, s15, 0x1900
	s_add_u32 s23, s23, 0x11000
	v_add_u32_e32 v44, s23, v44
	v_add_u32_e32 v45, s23, v45
	v_add_u32_e32 v47, s23, v1
	ds_write_b128 v47, v[2:5] offset:4096
	ds_write_b128 v47, v[2:5] offset:5120
	s_waitcnt vmcnt(8)
	ds_write_b128 v44, v[48:51]
	ds_write_b128 v45, v[52:55]
	ds_write_b128 v44, v[56:59] offset:2048
	ds_write_b128 v45, v[60:63] offset:2048
	v_cvt_f16_f32_e32 v42, v42
	v_cvt_f16_f32_e32 v43, v43
	s_mov_b32 s28, 0x5040100
	v_perm_b32 v42, v42, v42, s28
	v_perm_b32 v43, v43, v43, s28
	v_lshrrev_b32_e32 v44, 5, v46
	v_and_b32_e32 v45, 15, v46
	v_bfe_u32 v47, v46, 4, 1
	v_cmp_eq_u32_e32 vcc, v45, v47
	v_lshlrev_b32_e32 v44, 4, v44
	v_add_u32_e32 v46, s23, v44
	v_add_u32_e32 v45, 0x800, v46
	v_mov_b32_e32 v47, s23
	v_add_u32_e32 v47, 0x1000, v47
	v_cndmask_b32_e32 v47, v47, v45, vcc
	s_waitcnt lgkmcnt(0)
	ds_read_b128 v[144:147], v46
	ds_read_b128 v[148:151], v46 offset:32
	ds_read_b128 v[160:163], v47
	ds_read_b128 v[152:155], v46 offset:64
	ds_read_b128 v[164:167], v47 offset:32
	s_add_u32 s27, s17, 8
	s_lshl_b32 s27, s27, 10
	s_add_u32 s29, s17, 63
	s_lshl_b32 s29, s29, 10
	s_movk_i32 s28, 0x400
	s_mov_b32 s26, 0
	s_waitcnt lgkmcnt(4)
	v_pk_max_u16 v128, v144, v42
	v_pk_max_u16 v129, v145, v42
	v_pk_max_u16 v130, v146, v42
	v_pk_max_u16 v131, v147, v42
	v_pk_max_u16 v136, v144, v43
	v_pk_max_u16 v137, v145, v43
	v_pk_max_u16 v138, v146, v43
	v_pk_max_u16 v139, v147, v43
	s_mov_b32 s31, 0xfc00
	s_cmp_ge_u32 s15, 4
	s_cbranch_scc0 .Lk2_noprio
	s_setprio 1
.Lk2_noprio:
.Lk2_loop:
	s_and_b32 s23, s27, s31
	s_add_u32 s24, s20, s23
	s_addc_u32 s25, s21, 0
	s_add_u32 s27, s27, s28
	s_waitcnt vmcnt(7)
	s_waitcnt lgkmcnt(2)
	v_mfma_f32_32x32x16_f16 a[0:15], v[64:67], v[128:131], a[0:15]
	v_pk_max_u16 v132, v148, v42
	v_pk_max_u16 v133, v149, v42
	v_pk_max_u16 v134, v150, v42
	v_pk_max_u16 v135, v151, v42
	v_mfma_f32_32x32x16_f16 a[16:31], v[64:67], v[136:139], a[16:31]
	v_pk_max_u16 v140, v148, v43
	v_pk_max_u16 v141, v149, v43
	v_pk_max_u16 v142, v150, v43
	v_pk_max_u16 v143, v151, v43
	v_mfma_f32_16x16x32_f16 a[32:35], v[160:163], v[128:131], a[32:35]
	global_load_dwordx4 v[64:67], v1, s[24:25]
	ds_read_b128 v[156:159], v46 offset:96
	ds_read_b128 v[168:171], v47 offset:64
	v_mfma_f32_16x16x32_f16 a[36:39], v[160:163], v[136:139], a[36:39]
	s_and_b32 s23, s27, s31
	s_add_u32 s24, s20, s23
	s_addc_u32 s25, s21, 0
	s_add_u32 s27, s27, s28
	s_waitcnt vmcnt(7)
	s_waitcnt lgkmcnt(2)
	v_mfma_f32_32x32x16_f16 a[0:15], v[68:71], v[132:135], a[0:15]
	v_pk_max_u16 v128, v152, v42
	v_pk_max_u16 v129, v153, v42
	v_pk_max_u16 v130, v154, v42
	v_pk_max_u16 v131, v155, v42
	v_mfma_f32_32x32x16_f16 a[16:31], v[68:71], v[140:143], a[16:31]
	v_pk_max_u16 v136, v152, v43
	v_pk_max_u16 v137, v153, v43
	v_pk_max_u16 v138, v154, v43
	v_pk_max_u16 v139, v155, v43
	v_mfma_f32_16x16x32_f16 a[32:35], v[164:167], v[132:135], a[32:35]
	global_load_dwordx4 v[68:71], v1, s[24:25]
	ds_read_b128 v[144:147], v46 offset:128
	ds_read_b128 v[172:175], v47 offset:96
	v_mfma_f32_16x16x32_f16 a[36:39], v[164:167], v[140:143], a[36:39]
	s_and_b32 s23, s27, s31
	s_add_u32 s24, s20, s23
	s_addc_u32 s25, s21, 0
	s_add_u32 s27, s27, s28
	s_waitcnt vmcnt(7)
	s_waitcnt lgkmcnt(2)
	v_mfma_f32_32x32x16_f16 a[0:15], v[72:75], v[128:131], a[0:15]
	v_pk_max_u16 v132, v156, v42
	v_pk_max_u16 v133, v157, v42
	v_pk_max_u16 v134, v158, v42
	v_pk_max_u16 v135, v159, v42
	v_mfma_f32_32x32x16_f16 a[16:31], v[72:75], v[136:139], a[16:31]
	v_pk_max_u16 v140, v156, v43
	v_pk_max_u16 v141, v157, v43
	v_pk_max_u16 v142, v158, v43
	v_pk_max_u16 v143, v159, v43
	v_mfma_f32_16x16x32_f16 a[32:35], v[168:171], v[128:131], a[32:35]
	global_load_dwordx4 v[72:75], v1, s[24:25]
	ds_read_b128 v[148:151], v46 offset:160
	ds_read_b128 v[160:163], v47 offset:128
	v_mfma_f32_16x16x32_f16 a[36:39], v[168:171], v[136:139], a[36:39]
	s_and_b32 s23, s27, s31
	s_add_u32 s24, s20, s23
	s_addc_u32 s25, s21, 0
	s_add_u32 s27, s27, s28
	s_waitcnt vmcnt(7)
	s_waitcnt lgkmcnt(2)
	v_mfma_f32_32x32x16_f16 a[0:15], v[76:79], v[132:135], a[0:15]
	v_pk_max_u16 v128, v144, v42
	v_pk_max_u16 v129, v145, v42
	v_pk_max_u16 v130, v146, v42
	v_pk_max_u16 v131, v147, v42
	v_mfma_f32_32x32x16_f16 a[16:31], v[76:79], v[140:143], a[16:31]
	v_pk_max_u16 v136, v144, v43
	v_pk_max_u16 v137, v145, v43
	v_pk_max_u16 v138, v146, v43
	v_pk_max_u16 v139, v147, v43
	v_mfma_f32_16x16x32_f16 a[32:35], v[172:175], v[132:135], a[32:35]
	global_load_dwordx4 v[76:79], v1, s[24:25]
	ds_read_b128 v[152:155], v46 offset:192
	ds_read_b128 v[164:167], v47 offset:160
	v_mfma_f32_16x16x32_f16 a[36:39], v[172:175], v[140:143], a[36:39]
	s_and_b32 s23, s27, s31
	s_add_u32 s24, s20, s23
	s_addc_u32 s25, s21, 0
	s_add_u32 s27, s27, s28
	s_waitcnt vmcnt(7)
	s_waitcnt lgkmcnt(2)
	v_mfma_f32_32x32x16_f16 a[0:15], v[80:83], v[128:131], a[0:15]
	v_pk_max_u16 v132, v148, v42
	v_pk_max_u16 v133, v149, v42
	v_pk_max_u16 v134, v150, v42
	v_pk_max_u16 v135, v151, v42
	v_mfma_f32_32x32x16_f16 a[16:31], v[80:83], v[136:139], a[16:31]
	v_pk_max_u16 v140, v148, v43
	v_pk_max_u16 v141, v149, v43
	v_pk_max_u16 v142, v150, v43
	v_pk_max_u16 v143, v151, v43
	v_mfma_f32_16x16x32_f16 a[32:35], v[160:163], v[128:131], a[32:35]
	global_load_dwordx4 v[80:83], v1, s[24:25]
	ds_read_b128 v[156:159], v46 offset:224
	ds_read_b128 v[168:171], v47 offset:192
	v_mfma_f32_16x16x32_f16 a[36:39], v[160:163], v[136:139], a[36:39]
	s_and_b32 s23, s27, s31
	s_add_u32 s24, s20, s23
	s_addc_u32 s25, s21, 0
	s_add_u32 s27, s27, s28
	s_waitcnt vmcnt(7)
	s_waitcnt lgkmcnt(2)
	v_mfma_f32_32x32x16_f16 a[0:15], v[84:87], v[132:135], a[0:15]
	v_pk_max_u16 v128, v152, v42
	v_pk_max_u16 v129, v153, v42
	v_pk_max_u16 v130, v154, v42
	v_pk_max_u16 v131, v155, v42
	v_mfma_f32_32x32x16_f16 a[16:31], v[84:87], v[140:143], a[16:31]
	v_pk_max_u16 v136, v152, v43
	v_pk_max_u16 v137, v153, v43
	v_pk_max_u16 v138, v154, v43
	v_pk_max_u16 v139, v155, v43
	v_mfma_f32_16x16x32_f16 a[32:35], v[164:167], v[132:135], a[32:35]
	global_load_dwordx4 v[84:87], v1, s[24:25]
	ds_read_b128 v[144:147], v46 offset:256
	ds_read_b128 v[172:175], v47 offset:224
	v_mfma_f32_16x16x32_f16 a[36:39], v[164:167], v[140:143], a[36:39]
	s_and_b32 s23, s27, s31
	s_add_u32 s24, s20, s23
	s_addc_u32 s25, s21, 0
	s_add_u32 s27, s27, s28
	s_waitcnt vmcnt(7)
	s_waitcnt lgkmcnt(2)
	v_mfma_f32_32x32x16_f16 a[0:15], v[88:91], v[128:131], a[0:15]
	v_pk_max_u16 v132, v156, v42
	v_pk_max_u16 v133, v157, v42
	v_pk_max_u16 v134, v158, v42
	v_pk_max_u16 v135, v159, v42
	v_mfma_f32_32x32x16_f16 a[16:31], v[88:91], v[136:139], a[16:31]
	v_pk_max_u16 v140, v156, v43
	v_pk_max_u16 v141, v157, v43
	v_pk_max_u16 v142, v158, v43
	v_pk_max_u16 v143, v159, v43
	v_mfma_f32_16x16x32_f16 a[32:35], v[168:171], v[128:131], a[32:35]
	global_load_dwordx4 v[88:91], v1, s[24:25]
	ds_read_b128 v[148:151], v46 offset:288
	ds_read_b128 v[160:163], v47 offset:256
	v_mfma_f32_16x16x32_f16 a[36:39], v[168:171], v[136:139], a[36:39]
	s_and_b32 s23, s27, s31
	s_add_u32 s24, s20, s23
	s_addc_u32 s25, s21, 0
	s_add_u32 s27, s27, s28
	s_waitcnt vmcnt(7)
	s_waitcnt lgkmcnt(2)
	v_mfma_f32_32x32x16_f16 a[0:15], v[92:95], v[132:135], a[0:15]
	v_pk_max_u16 v128, v144, v42
	v_pk_max_u16 v129, v145, v42
	v_pk_max_u16 v130, v146, v42
	v_pk_max_u16 v131, v147, v42
	v_mfma_f32_32x32x16_f16 a[16:31], v[92:95], v[140:143], a[16:31]
	v_pk_max_u16 v136, v144, v43
	v_pk_max_u16 v137, v145, v43
	v_pk_max_u16 v138, v146, v43
	v_pk_max_u16 v139, v147, v43
	v_mfma_f32_16x16x32_f16 a[32:35], v[172:175], v[132:135], a[32:35]
	global_load_dwordx4 v[92:95], v1, s[24:25]
	ds_read_b128 v[152:155], v46 offset:320
	ds_read_b128 v[164:167], v47 offset:288
	v_mfma_f32_16x16x32_f16 a[36:39], v[172:175], v[140:143], a[36:39]
	s_add_u32 s26, s26, 1
	v_add_u32_e32 v46, 256, v46
	v_add_u32_e32 v47, 256, v47
	s_cmp_eq_u32 s26, 7
	s_cselect_b32 s27, s29, s27
	s_cselect_b32 s28, 0, s28
	s_cmp_lt_u32 s26, 8
	s_cbranch_scc1 .Lk2_loop
	v_and_b32_e32 v2, 63, v0
	v_lshrrev_b32_e32 v3, 5, v2
	v_and_b32_e32 v4, 31, v0
	s_lshl_b32 s23, s15, 4
	v_add_u32_e32 v3, s23, v3
	v_mul_u32_u24_e32 v3, 0x210, v3
	v_lshl_add_u32 v3, v4, 4, v3
	v_cmp_gt_u32_e32 vcc, 16, v2
	ds_write_b128 v3, a[0:3]
	ds_write_b128 v3, a[16:19] offset:4224
	ds_write_b128 v3, a[4:7] offset:1056
	ds_write_b128 v3, a[20:23] offset:5280
	ds_write_b128 v3, a[8:11] offset:2112
	ds_write_b128 v3, a[24:27] offset:6336
	ds_write_b128 v3, a[12:15] offset:3168
	ds_write_b128 v3, a[28:31] offset:7392
	s_and_saveexec_b64 s[2:3], vcc
	s_cbranch_execz .Lk2_nodred
	v_lshlrev_b32_e32 v5, 2, v2
	s_lshl_b32 s23, s15, 8
	v_add_u32_e32 v5, s23, v5
	v_add_u32_e32 v5, 0x10800, v5
	ds_write2_b32 v5, a32, a33 offset1:16
	ds_write2_b32 v5, a36, a37 offset0:32 offset1:48
